# spmm kernels: every wave ranks its block's 32 rows by length (LDS) and groups take rows in that order, so rows walked in lock-step have similar lengths (fewer padded batches); rowptr values reused fro
# speedup vs baseline: 1.0499x; 1.0219x over previous
.Lperm_skip0:
	s_not_b32 s2, s2
	s_add_i32 s12, s3, s2
	v_bfe_u32 v2, v0, 4, 2
	s_lshl_b32 s2, s12, 5
	v_and_b32_e32 v3, 28, v1
	s_load_dwordx2 s[8:9], s[0:1], 0x0
	v_mbcnt_lo_u32_b32 v5, -1, 0
	v_mbcnt_hi_u32_b32 v5, -1, v5
	v_min_u32_e32 v6, 32, v5
	v_add_u32_e32 v6, s2, v6
	v_min_i32_e32 v6, s4, v6
	v_lshlrev_b32_e32 v7, 2, v6
	v_lshrrev_b32_e32 v9, 6, v0
	v_lshlrev_b32_e32 v9, 9, v9
	v_lshlrev_b32_e32 v10, 2, v5
	v_add_u32_e32 v11, v9, v10
	s_waitcnt lgkmcnt(0)
	global_load_dword v8, v7, s[8:9]
	v_cmp_gt_u32_e32 vcc, 33, v5
	s_waitcnt vmcnt(0)
	s_and_saveexec_b64 s[10:11], vcc
	ds_write_b32 v11, v8 offset:16448
	s_mov_b64 exec, s[10:11]
	ds_read_b32 v12, v11 offset:16452
	v_sub_u32_e32 v13, 31, v5
	s_waitcnt lgkmcnt(0)
	v_sub_u32_e32 v12, v12, v8
	v_lshl_add_u32 v12, v12, 5, v13
	v_cmp_gt_u32_e32 vcc, 32, v5
	s_and_saveexec_b64 s[10:11], vcc
	ds_write_b32 v11, v12 offset:16608
	s_mov_b64 exec, s[10:11]
	v_mov_b32_e32 v13, 0
	ds_read_b128 v[14:17], v9 offset:16608
	s_waitcnt lgkmcnt(0)
	v_sub_u32_e32 v6, v12, v14
	v_ashrrev_i32_e32 v6, 31, v6
	v_sub_u32_e32 v13, v13, v6
	v_sub_u32_e32 v6, v12, v15
	v_ashrrev_i32_e32 v6, 31, v6
	v_sub_u32_e32 v13, v13, v6
	v_sub_u32_e32 v6, v12, v16
	v_ashrrev_i32_e32 v6, 31, v6
	v_sub_u32_e32 v13, v13, v6
	v_sub_u32_e32 v6, v12, v17
	v_ashrrev_i32_e32 v6, 31, v6
	v_sub_u32_e32 v13, v13, v6
	ds_read_b128 v[14:17], v9 offset:16624
	s_waitcnt lgkmcnt(0)
	v_sub_u32_e32 v6, v12, v14
	v_ashrrev_i32_e32 v6, 31, v6
	v_sub_u32_e32 v13, v13, v6
	v_sub_u32_e32 v6, v12, v15
	v_ashrrev_i32_e32 v6, 31, v6
	v_sub_u32_e32 v13, v13, v6
	v_sub_u32_e32 v6, v12, v16
	v_ashrrev_i32_e32 v6, 31, v6
	v_sub_u32_e32 v13, v13, v6
	v_sub_u32_e32 v6, v12, v17
	v_ashrrev_i32_e32 v6, 31, v6
	v_sub_u32_e32 v13, v13, v6
	ds_read_b128 v[14:17], v9 offset:16640
	s_waitcnt lgkmcnt(0)
	v_sub_u32_e32 v6, v12, v14
	v_ashrrev_i32_e32 v6, 31, v6
	v_sub_u32_e32 v13, v13, v6
	v_sub_u32_e32 v6, v12, v15
	v_ashrrev_i32_e32 v6, 31, v6
	v_sub_u32_e32 v13, v13, v6
	v_sub_u32_e32 v6, v12, v16
	v_ashrrev_i32_e32 v6, 31, v6
	v_sub_u32_e32 v13, v13, v6
	v_sub_u32_e32 v6, v12, v17
	v_ashrrev_i32_e32 v6, 31, v6
	v_sub_u32_e32 v13, v13, v6
	ds_read_b128 v[14:17], v9 offset:16656
	s_waitcnt lgkmcnt(0)
	v_sub_u32_e32 v6, v12, v14
	v_ashrrev_i32_e32 v6, 31, v6
	v_sub_u32_e32 v13, v13, v6
	v_sub_u32_e32 v6, v12, v15
	v_ashrrev_i32_e32 v6, 31, v6
	v_sub_u32_e32 v13, v13, v6
	v_sub_u32_e32 v6, v12, v16
	v_ashrrev_i32_e32 v6, 31, v6
	v_sub_u32_e32 v13, v13, v6
	v_sub_u32_e32 v6, v12, v17
	v_ashrrev_i32_e32 v6, 31, v6
	v_sub_u32_e32 v13, v13, v6
	ds_read_b128 v[14:17], v9 offset:16672
	s_waitcnt lgkmcnt(0)
	v_sub_u32_e32 v6, v12, v14
	v_ashrrev_i32_e32 v6, 31, v6
	v_sub_u32_e32 v13, v13, v6
	v_sub_u32_e32 v6, v12, v15
	v_ashrrev_i32_e32 v6, 31, v6
	v_sub_u32_e32 v13, v13, v6
	v_sub_u32_e32 v6, v12, v16
	v_ashrrev_i32_e32 v6, 31, v6
	v_sub_u32_e32 v13, v13, v6
	v_sub_u32_e32 v6, v12, v17
	v_ashrrev_i32_e32 v6, 31, v6
	v_sub_u32_e32 v13, v13, v6
	ds_read_b128 v[14:17], v9 offset:16688
	s_waitcnt lgkmcnt(0)
	v_sub_u32_e32 v6, v12, v14
	v_ashrrev_i32_e32 v6, 31, v6
	v_sub_u32_e32 v13, v13, v6
	v_sub_u32_e32 v6, v12, v15
	v_ashrrev_i32_e32 v6, 31, v6
	v_sub_u32_e32 v13, v13, v6
	v_sub_u32_e32 v6, v12, v16
	v_ashrrev_i32_e32 v6, 31, v6
	v_sub_u32_e32 v13, v13, v6
	v_sub_u32_e32 v6, v12, v17
	v_ashrrev_i32_e32 v6, 31, v6
	v_sub_u32_e32 v13, v13, v6
	ds_read_b128 v[14:17], v9 offset:16704
	s_waitcnt lgkmcnt(0)
	v_sub_u32_e32 v6, v12, v14
	v_ashrrev_i32_e32 v6, 31, v6
	v_sub_u32_e32 v13, v13, v6
	v_sub_u32_e32 v6, v12, v15
	v_ashrrev_i32_e32 v6, 31, v6
	v_sub_u32_e32 v13, v13, v6
	v_sub_u32_e32 v6, v12, v16
	v_ashrrev_i32_e32 v6, 31, v6
	v_sub_u32_e32 v13, v13, v6
	v_sub_u32_e32 v6, v12, v17
	v_ashrrev_i32_e32 v6, 31, v6
	v_sub_u32_e32 v13, v13, v6
	ds_read_b128 v[14:17], v9 offset:16720
	s_waitcnt lgkmcnt(0)
	v_sub_u32_e32 v6, v12, v14
	v_ashrrev_i32_e32 v6, 31, v6
	v_sub_u32_e32 v13, v13, v6
	v_sub_u32_e32 v6, v12, v15
	v_ashrrev_i32_e32 v6, 31, v6
	v_sub_u32_e32 v13, v13, v6
	v_sub_u32_e32 v6, v12, v16
	v_ashrrev_i32_e32 v6, 31, v6
	v_sub_u32_e32 v13, v13, v6
	v_sub_u32_e32 v6, v12, v17
	v_ashrrev_i32_e32 v6, 31, v6
	v_sub_u32_e32 v13, v13, v6
	v_lshl_add_u32 v6, v13, 2, v9
	v_cmp_gt_u32_e32 vcc, 32, v5
	s_and_saveexec_b64 s[10:11], vcc
	ds_write_b32 v6, v5 offset:16768
	s_mov_b64 exec, s[10:11]
	v_bfe_u32 v6, v0, 4, 5
	v_lshl_add_u32 v6, v6, 2, v9
	ds_read_b32 v7, v6 offset:16768
	s_waitcnt lgkmcnt(0)
	v_add_u32_e32 v98, s2, v7
	v_lshl_add_u32 v7, v7, 2, v9
	ds_read_b32 v4, v7 offset:16448
	ds_read_b32 v6, v7 offset:16452
	v_ashrrev_i32_e32 v99, 31, v98
	v_mov_b32_e32 v2, 0
	s_waitcnt lgkmcnt(0)
	v_sub_u32_e32 v101, v6, v4
	v_cmp_gt_i32_e64 s[2:3], s4, v98
	s_mov_b64 s[4:5], exec
	s_nop 1
	v_cndmask_b32_e64 v4, 0, v4, s[2:3]
	v_cndmask_b32_e64 v101, 0, v101, s[2:3]

	.amdhsa_kernel _Z6k_spmmILb0ELi0EEvPKiPK15HIP_vector_typeIiLj2EEPKvPKfPKDF16_S9_S9_iPfPDF16_PhSC_PKhS9_SG_S9_S9_i
		.amdhsa_group_segment_fixed_size 20544
		.amdhsa_private_segment_fixed_size 0
		.amdhsa_kernarg_size 400
		.amdhsa_user_sgpr_count 2
		.amdhsa_user_sgpr_dispatch_ptr 0
		.amdhsa_user_sgpr_queue_ptr 0
		.amdhsa_user_sgpr_kernarg_segment_ptr 1
		.amdhsa_user_sgpr_dispatch_id 0
		.amdhsa_user_sgpr_kernarg_preload_length 0
		.amdhsa_user_sgpr_kernarg_preload_offset 0
		.amdhsa_user_sgpr_private_segment_size 0
		.amdhsa_uses_dynamic_stack 0
		.amdhsa_enable_private_segment 0
		.amdhsa_system_sgpr_workgroup_id_x 1
		.amdhsa_system_sgpr_workgroup_id_y 0
		.amdhsa_system_sgpr_workgroup_id_z 0
		.amdhsa_system_sgpr_workgroup_info 0
		.amdhsa_system_vgpr_workitem_id 0
		.amdhsa_next_free_vgpr 128
		.amdhsa_next_free_sgpr 30
		.amdhsa_accum_offset 128
		.amdhsa_reserve_vcc 1
		.amdhsa_float_round_mode_32 0
		.amdhsa_float_round_mode_16_64 0
		.amdhsa_float_denorm_mode_32 3
		.amdhsa_float_denorm_mode_16_64 3
		.amdhsa_dx10_clamp 1
		.amdhsa_ieee_mode 1
		.amdhsa_fp16_overflow 0
		.amdhsa_tg_split 0
		.amdhsa_exception_fp_ieee_invalid_op 0
		.amdhsa_exception_fp_denorm_src 0
		.amdhsa_exception_fp_ieee_div_zero 0
		.amdhsa_exception_fp_ieee_overflow 0
		.amdhsa_exception_fp_ieee_underflow 0
		.amdhsa_exception_fp_ieee_inexact 0
		.amdhsa_exception_int_div_zero 0
	.end_amdhsa_kernel

_Z6k_spmmILb1ELi1EEvPKiPK15HIP_vector_typeIiLj2EEPKvPKfPKDF16_S9_S9_iPfPDF16_PhSC_PKhS9_SG_S9_S9_i:
	s_load_dword s3, s[0:1], 0x90
	s_load_dwordx2 s[14:15], s[0:1], 0x8
	s_load_dword s4, s[0:1], 0x38
	s_not_b32 s2, s2
	v_lshrrev_b32_e32 v2, 4, v0
	s_waitcnt lgkmcnt(0)
	s_add_i32 s6, s3, s2
	v_bfe_u32 v1, v0, 4, 2
	s_lshl_b32 s2, s6, 5
	v_and_b32_e32 v2, 28, v2
	s_load_dwordx2 s[8:9], s[0:1], 0x0
	v_mbcnt_lo_u32_b32 v5, -1, 0
	v_mbcnt_hi_u32_b32 v5, -1, v5
	v_min_u32_e32 v6, 32, v5
	v_add_u32_e32 v6, s2, v6
	v_min_i32_e32 v6, s4, v6
	v_lshlrev_b32_e32 v7, 2, v6
	v_lshrrev_b32_e32 v9, 6, v0
	v_lshlrev_b32_e32 v9, 9, v9
	v_lshlrev_b32_e32 v10, 2, v5
	v_add_u32_e32 v11, v9, v10
	s_waitcnt lgkmcnt(0)
	global_load_dword v8, v7, s[8:9]
	v_cmp_gt_u32_e32 vcc, 33, v5
	s_waitcnt vmcnt(0)
	s_and_saveexec_b64 s[10:11], vcc
	ds_write_b32 v11, v8 offset:16448
	s_mov_b64 exec, s[10:11]
	ds_read_b32 v12, v11 offset:16452
	v_sub_u32_e32 v13, 31, v5
	s_waitcnt lgkmcnt(0)
	v_sub_u32_e32 v12, v12, v8
	v_lshl_add_u32 v12, v12, 5, v13
	v_cmp_gt_u32_e32 vcc, 32, v5
	s_and_saveexec_b64 s[10:11], vcc
	ds_write_b32 v11, v12 offset:16608
	s_mov_b64 exec, s[10:11]
	v_mov_b32_e32 v13, 0
	ds_read_b128 v[14:17], v9 offset:16608
	s_waitcnt lgkmcnt(0)
	v_sub_u32_e32 v6, v12, v14
	v_ashrrev_i32_e32 v6, 31, v6
	v_sub_u32_e32 v13, v13, v6
	v_sub_u32_e32 v6, v12, v15
	v_ashrrev_i32_e32 v6, 31, v6
	v_sub_u32_e32 v13, v13, v6
	v_sub_u32_e32 v6, v12, v16
	v_ashrrev_i32_e32 v6, 31, v6
	v_sub_u32_e32 v13, v13, v6
	v_sub_u32_e32 v6, v12, v17
	v_ashrrev_i32_e32 v6, 31, v6
	v_sub_u32_e32 v13, v13, v6
	ds_read_b128 v[14:17], v9 offset:16624
	s_waitcnt lgkmcnt(0)
	v_sub_u32_e32 v6, v12, v14
	v_ashrrev_i32_e32 v6, 31, v6
	v_sub_u32_e32 v13, v13, v6
	v_sub_u32_e32 v6, v12, v15
	v_ashrrev_i32_e32 v6, 31, v6
	v_sub_u32_e32 v13, v13, v6
	v_sub_u32_e32 v6, v12, v16
	v_ashrrev_i32_e32 v6, 31, v6
	v_sub_u32_e32 v13, v13, v6
	v_sub_u32_e32 v6, v12, v17
	v_ashrrev_i32_e32 v6, 31, v6
	v_sub_u32_e32 v13, v13, v6
	ds_read_b128 v[14:17], v9 offset:16640
	s_waitcnt lgkmcnt(0)
	v_sub_u32_e32 v6, v12, v14
	v_ashrrev_i32_e32 v6, 31, v6
	v_sub_u32_e32 v13, v13, v6
	v_sub_u32_e32 v6, v12, v15
	v_ashrrev_i32_e32 v6, 31, v6
	v_sub_u32_e32 v13, v13, v6
	v_sub_u32_e32 v6, v12, v16
	v_ashrrev_i32_e32 v6, 31, v6
	v_sub_u32_e32 v13, v13, v6
	v_sub_u32_e32 v6, v12, v17
	v_ashrrev_i32_e32 v6, 31, v6
	v_sub_u32_e32 v13, v13, v6
	ds_read_b128 v[14:17], v9 offset:16656
	s_waitcnt lgkmcnt(0)
	v_sub_u32_e32 v6, v12, v14
	v_ashrrev_i32_e32 v6, 31, v6
	v_sub_u32_e32 v13, v13, v6
	v_sub_u32_e32 v6, v12, v15
	v_ashrrev_i32_e32 v6, 31, v6
	v_sub_u32_e32 v13, v13, v6
	v_sub_u32_e32 v6, v12, v16
	v_ashrrev_i32_e32 v6, 31, v6
	v_sub_u32_e32 v13, v13, v6
	v_sub_u32_e32 v6, v12, v17
	v_ashrrev_i32_e32 v6, 31, v6
	v_sub_u32_e32 v13, v13, v6
	ds_read_b128 v[14:17], v9 offset:16672
	s_waitcnt lgkmcnt(0)
	v_sub_u32_e32 v6, v12, v14
	v_ashrrev_i32_e32 v6, 31, v6
	v_sub_u32_e32 v13, v13, v6
	v_sub_u32_e32 v6, v12, v15
	v_ashrrev_i32_e32 v6, 31, v6
	v_sub_u32_e32 v13, v13, v6
	v_sub_u32_e32 v6, v12, v16
	v_ashrrev_i32_e32 v6, 31, v6
	v_sub_u32_e32 v13, v13, v6
	v_sub_u32_e32 v6, v12, v17
	v_ashrrev_i32_e32 v6, 31, v6
	v_sub_u32_e32 v13, v13, v6
	ds_read_b128 v[14:17], v9 offset:16688
	s_waitcnt lgkmcnt(0)
	v_sub_u32_e32 v6, v12, v14
	v_ashrrev_i32_e32 v6, 31, v6
	v_sub_u32_e32 v13, v13, v6
	v_sub_u32_e32 v6, v12, v15
	v_ashrrev_i32_e32 v6, 31, v6
	v_sub_u32_e32 v13, v13, v6
	v_sub_u32_e32 v6, v12, v16
	v_ashrrev_i32_e32 v6, 31, v6
	v_sub_u32_e32 v13, v13, v6
	v_sub_u32_e32 v6, v12, v17
	v_ashrrev_i32_e32 v6, 31, v6
	v_sub_u32_e32 v13, v13, v6
	ds_read_b128 v[14:17], v9 offset:16704
	s_waitcnt lgkmcnt(0)
	v_sub_u32_e32 v6, v12, v14
	v_ashrrev_i32_e32 v6, 31, v6
	v_sub_u32_e32 v13, v13, v6
	v_sub_u32_e32 v6, v12, v15
	v_ashrrev_i32_e32 v6, 31, v6
	v_sub_u32_e32 v13, v13, v6
	v_sub_u32_e32 v6, v12, v16
	v_ashrrev_i32_e32 v6, 31, v6
	v_sub_u32_e32 v13, v13, v6
	v_sub_u32_e32 v6, v12, v17
	v_ashrrev_i32_e32 v6, 31, v6
	v_sub_u32_e32 v13, v13, v6
	ds_read_b128 v[14:17], v9 offset:16720
	s_waitcnt lgkmcnt(0)
	v_sub_u32_e32 v6, v12, v14
	v_ashrrev_i32_e32 v6, 31, v6
	v_sub_u32_e32 v13, v13, v6
	v_sub_u32_e32 v6, v12, v15
	v_ashrrev_i32_e32 v6, 31, v6
	v_sub_u32_e32 v13, v13, v6
	v_sub_u32_e32 v6, v12, v16
	v_ashrrev_i32_e32 v6, 31, v6
	v_sub_u32_e32 v13, v13, v6
	v_sub_u32_e32 v6, v12, v17
	v_ashrrev_i32_e32 v6, 31, v6
	v_sub_u32_e32 v13, v13, v6
	v_lshl_add_u32 v6, v13, 2, v9
	v_cmp_gt_u32_e32 vcc, 32, v5
	s_and_saveexec_b64 s[10:11], vcc
	ds_write_b32 v6, v5 offset:16768
	s_mov_b64 exec, s[10:11]
	v_bfe_u32 v6, v0, 4, 5
	v_lshl_add_u32 v6, v6, 2, v9
	ds_read_b32 v7, v6 offset:16768
	s_waitcnt lgkmcnt(0)
	v_add_u32_e32 v18, s2, v7
	v_lshl_add_u32 v7, v7, 2, v9
	ds_read_b32 v4, v7 offset:16448
	ds_read_b32 v6, v7 offset:16452
	v_ashrrev_i32_e32 v19, 31, v18
	v_mov_b32_e32 v2, 0
	s_waitcnt lgkmcnt(0)
	v_sub_u32_e32 v55, v6, v4
	v_cmp_gt_i32_e64 s[2:3], s4, v18
	s_mov_b64 s[4:5], exec
	s_nop 1
	v_cndmask_b32_e64 v4, 0, v4, s[2:3]
	v_cndmask_b32_e64 v55, 0, v55, s[2:3]

	.amdhsa_kernel _Z6k_spmmILb1ELi1EEvPKiPK15HIP_vector_typeIiLj2EEPKvPKfPKDF16_S9_S9_iPfPDF16_PhSC_PKhS9_SG_S9_S9_i
		.amdhsa_group_segment_fixed_size 20544
		.amdhsa_private_segment_fixed_size 0
		.amdhsa_kernarg_size 400
		.amdhsa_user_sgpr_count 2
		.amdhsa_user_sgpr_dispatch_ptr 0
		.amdhsa_user_sgpr_queue_ptr 0
		.amdhsa_user_sgpr_kernarg_segment_ptr 1
		.amdhsa_user_sgpr_dispatch_id 0
		.amdhsa_user_sgpr_kernarg_preload_length 0
		.amdhsa_user_sgpr_kernarg_preload_offset 0
		.amdhsa_user_sgpr_private_segment_size 0
		.amdhsa_uses_dynamic_stack 0
		.amdhsa_enable_private_segment 0
		.amdhsa_system_sgpr_workgroup_id_x 1
		.amdhsa_system_sgpr_workgroup_id_y 0
		.amdhsa_system_sgpr_workgroup_id_z 0
		.amdhsa_system_sgpr_workgroup_info 0
		.amdhsa_system_vgpr_workitem_id 0
		.amdhsa_next_free_vgpr 64
		.amdhsa_next_free_sgpr 30
		.amdhsa_accum_offset 64
		.amdhsa_reserve_vcc 1
		.amdhsa_float_round_mode_32 0
		.amdhsa_float_round_mode_16_64 0
		.amdhsa_float_denorm_mode_32 3
		.amdhsa_float_denorm_mode_16_64 3
		.amdhsa_dx10_clamp 1
		.amdhsa_ieee_mode 1
		.amdhsa_fp16_overflow 0
		.amdhsa_tg_split 0
		.amdhsa_exception_fp_ieee_invalid_op 0
		.amdhsa_exception_fp_denorm_src 0
		.amdhsa_exception_fp_ieee_div_zero 0
		.amdhsa_exception_fp_ieee_overflow 0
		.amdhsa_exception_fp_ieee_underflow 0
		.amdhsa_exception_fp_ieee_inexact 0
		.amdhsa_exception_int_div_zero 0
	.end_amdhsa_kernel

_Z6k_spmmILb1ELi2EEvPKiPK15HIP_vector_typeIiLj2EEPKvPKfPKDF16_S9_S9_iPfPDF16_PhSC_PKhS9_SG_S9_S9_i:
	s_load_dword s3, s[0:1], 0x90
	s_load_dwordx2 s[6:7], s[0:1], 0x8
	s_load_dword s4, s[0:1], 0x38
	v_lshrrev_b32_e32 v1, 4, v0
	s_not_b32 s2, s2
	s_waitcnt lgkmcnt(0)
	s_add_i32 s16, s3, s2
	v_and_b32_e32 v2, 28, v1
	v_lshl_or_b32 v50, s16, 5, v2
	s_lshl_b32 s5, s16, 5
	s_load_dwordx2 s[8:9], s[0:1], 0x0
	v_mbcnt_lo_u32_b32 v20, -1, 0
	v_mbcnt_hi_u32_b32 v20, -1, v20
	v_min_u32_e32 v21, 32, v20
	v_add_u32_e32 v21, s5, v21
	v_min_i32_e32 v21, s4, v21
	v_lshlrev_b32_e32 v22, 2, v21
	v_lshrrev_b32_e32 v24, 6, v0
	v_lshlrev_b32_e32 v24, 9, v24
	v_lshlrev_b32_e32 v25, 2, v20
	v_add_u32_e32 v26, v24, v25
	s_waitcnt lgkmcnt(0)
	global_load_dword v23, v22, s[8:9]
	v_cmp_gt_u32_e32 vcc, 33, v20
	s_waitcnt vmcnt(0)
	s_and_saveexec_b64 s[10:11], vcc
	ds_write_b32 v26, v23 offset:16384
	s_mov_b64 exec, s[10:11]
	ds_read_b32 v27, v26 offset:16388
	v_sub_u32_e32 v28, 31, v20
	s_waitcnt lgkmcnt(0)
	v_sub_u32_e32 v27, v27, v23
	v_lshl_add_u32 v27, v27, 5, v28
	v_cmp_gt_u32_e32 vcc, 32, v20
	s_and_saveexec_b64 s[10:11], vcc
	ds_write_b32 v26, v27 offset:16544
	s_mov_b64 exec, s[10:11]
	v_mov_b32_e32 v28, 0
	ds_read_b128 v[30:33], v24 offset:16544
	s_waitcnt lgkmcnt(0)
	v_sub_u32_e32 v21, v27, v30
	v_ashrrev_i32_e32 v21, 31, v21
	v_sub_u32_e32 v28, v28, v21
	v_sub_u32_e32 v21, v27, v31
	v_ashrrev_i32_e32 v21, 31, v21
	v_sub_u32_e32 v28, v28, v21
	v_sub_u32_e32 v21, v27, v32
	v_ashrrev_i32_e32 v21, 31, v21
	v_sub_u32_e32 v28, v28, v21
	v_sub_u32_e32 v21, v27, v33
	v_ashrrev_i32_e32 v21, 31, v21
	v_sub_u32_e32 v28, v28, v21
	ds_read_b128 v[30:33], v24 offset:16560
	s_waitcnt lgkmcnt(0)
	v_sub_u32_e32 v21, v27, v30
	v_ashrrev_i32_e32 v21, 31, v21
	v_sub_u32_e32 v28, v28, v21
	v_sub_u32_e32 v21, v27, v31
	v_ashrrev_i32_e32 v21, 31, v21
	v_sub_u32_e32 v28, v28, v21
	v_sub_u32_e32 v21, v27, v32
	v_ashrrev_i32_e32 v21, 31, v21
	v_sub_u32_e32 v28, v28, v21
	v_sub_u32_e32 v21, v27, v33
	v_ashrrev_i32_e32 v21, 31, v21
	v_sub_u32_e32 v28, v28, v21
	ds_read_b128 v[30:33], v24 offset:16576
	s_waitcnt lgkmcnt(0)
	v_sub_u32_e32 v21, v27, v30
	v_ashrrev_i32_e32 v21, 31, v21
	v_sub_u32_e32 v28, v28, v21
	v_sub_u32_e32 v21, v27, v31
	v_ashrrev_i32_e32 v21, 31, v21
	v_sub_u32_e32 v28, v28, v21
	v_sub_u32_e32 v21, v27, v32
	v_ashrrev_i32_e32 v21, 31, v21
	v_sub_u32_e32 v28, v28, v21
	v_sub_u32_e32 v21, v27, v33
	v_ashrrev_i32_e32 v21, 31, v21
	v_sub_u32_e32 v28, v28, v21
	ds_read_b128 v[30:33], v24 offset:16592
	s_waitcnt lgkmcnt(0)
	v_sub_u32_e32 v21, v27, v30
	v_ashrrev_i32_e32 v21, 31, v21
	v_sub_u32_e32 v28, v28, v21
	v_sub_u32_e32 v21, v27, v31
	v_ashrrev_i32_e32 v21, 31, v21
	v_sub_u32_e32 v28, v28, v21
	v_sub_u32_e32 v21, v27, v32
	v_ashrrev_i32_e32 v21, 31, v21
	v_sub_u32_e32 v28, v28, v21
	v_sub_u32_e32 v21, v27, v33
	v_ashrrev_i32_e32 v21, 31, v21
	v_sub_u32_e32 v28, v28, v21
	ds_read_b128 v[30:33], v24 offset:16608
	s_waitcnt lgkmcnt(0)
	v_sub_u32_e32 v21, v27, v30
	v_ashrrev_i32_e32 v21, 31, v21
	v_sub_u32_e32 v28, v28, v21
	v_sub_u32_e32 v21, v27, v31
	v_ashrrev_i32_e32 v21, 31, v21
	v_sub_u32_e32 v28, v28, v21
	v_sub_u32_e32 v21, v27, v32
	v_ashrrev_i32_e32 v21, 31, v21
	v_sub_u32_e32 v28, v28, v21
	v_sub_u32_e32 v21, v27, v33
	v_ashrrev_i32_e32 v21, 31, v21
	v_sub_u32_e32 v28, v28, v21
	ds_read_b128 v[30:33], v24 offset:16624
	s_waitcnt lgkmcnt(0)
	v_sub_u32_e32 v21, v27, v30
	v_ashrrev_i32_e32 v21, 31, v21
	v_sub_u32_e32 v28, v28, v21
	v_sub_u32_e32 v21, v27, v31
	v_ashrrev_i32_e32 v21, 31, v21
	v_sub_u32_e32 v28, v28, v21
	v_sub_u32_e32 v21, v27, v32
	v_ashrrev_i32_e32 v21, 31, v21
	v_sub_u32_e32 v28, v28, v21
	v_sub_u32_e32 v21, v27, v33
	v_ashrrev_i32_e32 v21, 31, v21
	v_sub_u32_e32 v28, v28, v21
	ds_read_b128 v[30:33], v24 offset:16640
	s_waitcnt lgkmcnt(0)
	v_sub_u32_e32 v21, v27, v30
	v_ashrrev_i32_e32 v21, 31, v21
	v_sub_u32_e32 v28, v28, v21
	v_sub_u32_e32 v21, v27, v31
	v_ashrrev_i32_e32 v21, 31, v21
	v_sub_u32_e32 v28, v28, v21
	v_sub_u32_e32 v21, v27, v32
	v_ashrrev_i32_e32 v21, 31, v21
	v_sub_u32_e32 v28, v28, v21
	v_sub_u32_e32 v21, v27, v33
	v_ashrrev_i32_e32 v21, 31, v21
	v_sub_u32_e32 v28, v28, v21
	ds_read_b128 v[30:33], v24 offset:16656
	s_waitcnt lgkmcnt(0)
	v_sub_u32_e32 v21, v27, v30
	v_ashrrev_i32_e32 v21, 31, v21
	v_sub_u32_e32 v28, v28, v21
	v_sub_u32_e32 v21, v27, v31
	v_ashrrev_i32_e32 v21, 31, v21
	v_sub_u32_e32 v28, v28, v21
	v_sub_u32_e32 v21, v27, v32
	v_ashrrev_i32_e32 v21, 31, v21
	v_sub_u32_e32 v28, v28, v21
	v_sub_u32_e32 v21, v27, v33
	v_ashrrev_i32_e32 v21, 31, v21
	v_sub_u32_e32 v28, v28, v21
	v_lshl_add_u32 v21, v28, 2, v24
	v_cmp_gt_u32_e32 vcc, 32, v20
	s_and_saveexec_b64 s[10:11], vcc
	ds_write_b32 v21, v20 offset:16704
	s_mov_b64 exec, s[10:11]
	v_bfe_u32 v21, v0, 4, 5
	v_lshl_add_u32 v21, v21, 2, v24
	ds_read_b32 v22, v21 offset:16704
	s_waitcnt lgkmcnt(0)
	v_add_u32_e32 v16, s5, v22
	v_lshl_add_u32 v22, v22, 2, v24
	ds_read_b32 v4, v22 offset:16384
	ds_read_b32 v21, v22 offset:16388
	v_ashrrev_i32_e32 v17, 31, v16
	s_waitcnt lgkmcnt(0)
	v_sub_u32_e32 v52, v21, v4
	v_cmp_gt_i32_e32 vcc, s4, v16
	s_mov_b64 s[2:3], exec
	s_nop 1
	v_cndmask_b32_e32 v4, 0, v4, vcc
	v_cndmask_b32_e32 v52, 0, v52, vcc

	.amdhsa_kernel _Z6k_spmmILb1ELi2EEvPKiPK15HIP_vector_typeIiLj2EEPKvPKfPKDF16_S9_S9_iPfPDF16_PhSC_PKhS9_SG_S9_S9_i
		.amdhsa_group_segment_fixed_size 20480
		.amdhsa_private_segment_fixed_size 0
		.amdhsa_kernarg_size 400
		.amdhsa_user_sgpr_count 2
		.amdhsa_user_sgpr_dispatch_ptr 0
		.amdhsa_user_sgpr_queue_ptr 0
		.amdhsa_user_sgpr_kernarg_segment_ptr 1
		.amdhsa_user_sgpr_dispatch_id 0
		.amdhsa_user_sgpr_kernarg_preload_length 0
		.amdhsa_user_sgpr_kernarg_preload_offset 0
		.amdhsa_user_sgpr_private_segment_size 0
		.amdhsa_uses_dynamic_stack 0
		.amdhsa_enable_private_segment 0
		.amdhsa_system_sgpr_workgroup_id_x 1
		.amdhsa_system_sgpr_workgroup_id_y 0
		.amdhsa_system_sgpr_workgroup_id_z 0
		.amdhsa_system_sgpr_workgroup_info 0
		.amdhsa_system_vgpr_workitem_id 0
		.amdhsa_next_free_vgpr 64
		.amdhsa_next_free_sgpr 36
		.amdhsa_accum_offset 64
		.amdhsa_reserve_vcc 1
		.amdhsa_float_round_mode_32 0
		.amdhsa_float_round_mode_16_64 0
		.amdhsa_float_denorm_mode_32 3
		.amdhsa_float_denorm_mode_16_64 3
		.amdhsa_dx10_clamp 1
		.amdhsa_ieee_mode 1
		.amdhsa_fp16_overflow 0
		.amdhsa_tg_split 0
		.amdhsa_exception_fp_ieee_invalid_op 0
		.amdhsa_exception_fp_denorm_src 0
		.amdhsa_exception_fp_ieee_div_zero 0
		.amdhsa_exception_fp_ieee_overflow 0
		.amdhsa_exception_fp_ieee_underflow 0
		.amdhsa_exception_fp_ieee_inexact 0
		.amdhsa_exception_int_div_zero 0
	.end_amdhsa_kernel

amdhsa.kernels:
  - .agpr_count:     0
    .args:
      - .actual_access:  read_only
        .address_space:  global
        .offset:         0
        .size:           8
        .value_kind:     global_buffer
      - .actual_access:  write_only
        .address_space:  global
        .offset:         8
        .size:           8
        .value_kind:     global_buffer
      - .offset:         16
        .size:           4
        .value_kind:     by_value
      - .offset:         20
        .size:           4
        .value_kind:     by_value
    .group_segment_fixed_size: 8192
    .kernarg_segment_align: 8
    .kernarg_segment_size: 24
    .language:       OpenCL C
    .language_version:
      - 2
      - 0
    .max_flat_workgroup_size: 1024
    .name:           _Z7k_bhistPKiPiii
    .private_segment_fixed_size: 0
    .sgpr_count:     24
    .sgpr_spill_count: 0
    .symbol:         _Z7k_bhistPKiPiii.kd
    .uniform_work_group_size: 1
    .uses_dynamic_stack: false
    .vgpr_count:     50
    .vgpr_spill_count: 0
    .wavefront_size: 64
  - .agpr_count:     0
    .args:
      - .address_space:  global
        .offset:         0
        .size:           8
        .value_kind:     global_buffer
      - .actual_access:  write_only
        .address_space:  global
        .offset:         8
        .size:           8
        .value_kind:     global_buffer
      - .offset:         16
        .size:           4
        .value_kind:     by_value
      - .offset:         20
        .size:           4
        .value_kind:     by_value
      - .offset:         24
        .size:           4
        .value_kind:     by_value
      - .actual_access:  read_only
        .address_space:  global
        .offset:         32
        .size:           8
        .value_kind:     global_buffer
      - .actual_access:  read_only
        .address_space:  global
        .offset:         40
        .size:           8
        .value_kind:     global_buffer
      - .offset:         48
        .size:           4
        .value_kind:     by_value
      - .offset:         52
        .size:           4
        .value_kind:     by_value
      - .actual_access:  write_only
        .address_space:  global
        .offset:         56
        .size:           8
        .value_kind:     global_buffer
      - .actual_access:  write_only
        .address_space:  global
        .offset:         64
        .size:           8
        .value_kind:     global_buffer
      - .actual_access:  write_only
        .address_space:  global
        .offset:         72
        .size:           8
        .value_kind:     global_buffer
    .group_segment_fixed_size: 4160
    .kernarg_segment_align: 8
    .kernarg_segment_size: 80
    .language:       OpenCL C
    .language_version:
      - 2
      - 0
    .max_flat_workgroup_size: 1024
    .name:           _Z12k_bscan_prepPiS_iiiPKfS1_iiPDF16_PfS3_
    .private_segment_fixed_size: 0
    .sgpr_count:     24
    .sgpr_spill_count: 0
    .symbol:         _Z12k_bscan_prepPiS_iiiPKfS1_iiPDF16_PfS3_.kd
    .uniform_work_group_size: 1
    .uses_dynamic_stack: false
    .vgpr_count:     28
    .vgpr_spill_count: 0
    .wavefront_size: 64
  - .agpr_count:     0
    .args:
      - .actual_access:  read_only
        .address_space:  global
        .offset:         0
        .size:           8
        .value_kind:     global_buffer
      - .actual_access:  read_only
        .address_space:  global
        .offset:         8
        .size:           8
        .value_kind:     global_buffer
      - .actual_access:  read_only
        .address_space:  global
        .offset:         16
        .size:           8
        .value_kind:     global_buffer
      - .actual_access:  read_only
        .address_space:  global
        .offset:         24
        .size:           8
        .value_kind:     global_buffer
      - .actual_access:  read_only
        .address_space:  global
        .offset:         32
        .size:           8
        .value_kind:     global_buffer
      - .actual_access:  write_only
        .address_space:  global
        .offset:         40
        .size:           8
        .value_kind:     global_buffer
      - .actual_access:  write_only
        .address_space:  global
        .offset:         48
        .size:           8
        .value_kind:     global_buffer
      - .offset:         56
        .size:           4
        .value_kind:     by_value
      - .offset:         60
        .size:           4
        .value_kind:     by_value
      - .offset:         64
        .size:           4
        .value_kind:     by_value
      - .offset:         72
        .size:           4
        .value_kind:     hidden_block_count_x
      - .offset:         76
        .size:           4
        .value_kind:     hidden_block_count_y
      - .offset:         80
        .size:           4
        .value_kind:     hidden_block_count_z
      - .offset:         84
        .size:           2
        .value_kind:     hidden_group_size_x
      - .offset:         86
        .size:           2
        .value_kind:     hidden_group_size_y
      - .offset:         88
        .size:           2
        .value_kind:     hidden_group_size_z
      - .offset:         90
        .size:           2
        .value_kind:     hidden_remainder_x
      - .offset:         92
        .size:           2
        .value_kind:     hidden_remainder_y
      - .offset:         94
        .size:           2
        .value_kind:     hidden_remainder_z
      - .offset:         112
        .size:           8
        .value_kind:     hidden_global_offset_x
      - .offset:         120
        .size:           8
        .value_kind:     hidden_global_offset_y
      - .offset:         128
        .size:           8
        .value_kind:     hidden_global_offset_z
      - .offset:         136
        .size:           2
        .value_kind:     hidden_grid_dims
    .group_segment_fixed_size: 154816
    .kernarg_segment_align: 8
    .kernarg_segment_size: 328
    .language:       OpenCL C
    .language_version:
      - 2
      - 0
    .max_flat_workgroup_size: 1024
    .name:           _Z4k_l1PKiS0_PKfS0_S0_PiP15HIP_vector_typeIiLj2EEiii
    .private_segment_fixed_size: 0
    .sgpr_count:     92
    .sgpr_spill_count: 0
    .symbol:         _Z4k_l1PKiS0_PKfS0_S0_PiP15HIP_vector_typeIiLj2EEiii.kd
    .uniform_work_group_size: 1
    .uses_dynamic_stack: false
    .vgpr_count:     128
    .vgpr_spill_count: 0
    .wavefront_size: 64
  - .agpr_count:     0
    .args:
      - .actual_access:  read_only
        .address_space:  global
        .offset:         0
        .size:           8
        .value_kind:     global_buffer
      - .actual_access:  read_only
        .address_space:  global
        .offset:         8
        .size:           8
        .value_kind:     global_buffer
      - .actual_access:  write_only
        .address_space:  global
        .offset:         16
        .size:           8
        .value_kind:     global_buffer
      - .actual_access:  write_only
        .address_space:  global
        .offset:         24
        .size:           8
        .value_kind:     global_buffer
      - .offset:         32
        .size:           4
        .value_kind:     by_value
      - .offset:         36
        .size:           4
        .value_kind:     by_value
      - .offset:         40
        .size:           4
        .value_kind:     hidden_block_count_x
      - .offset:         44
        .size:           4
        .value_kind:     hidden_block_count_y
      - .offset:         48
        .size:           4
        .value_kind:     hidden_block_count_z
      - .offset:         52
        .size:           2
        .value_kind:     hidden_group_size_x
      - .offset:         54
        .size:           2
        .value_kind:     hidden_group_size_y
      - .offset:         56
        .size:           2
        .value_kind:     hidden_group_size_z
      - .offset:         58
        .size:           2
        .value_kind:     hidden_remainder_x
      - .offset:         60
        .size:           2
        .value_kind:     hidden_remainder_y
      - .offset:         62
        .size:           2
        .value_kind:     hidden_remainder_z
      - .offset:         80
        .size:           8
        .value_kind:     hidden_global_offset_x
      - .offset:         88
        .size:           8
        .value_kind:     hidden_global_offset_y
      - .offset:         96
        .size:           8
        .value_kind:     hidden_global_offset_z
      - .offset:         104
        .size:           2
        .value_kind:     hidden_grid_dims
    .group_segment_fixed_size: 147520
    .kernarg_segment_align: 8
    .kernarg_segment_size: 296
    .language:       OpenCL C
    .language_version:
      - 2
      - 0
    .max_flat_workgroup_size: 1024
    .name:           _Z4k_l2PK15HIP_vector_typeIiLj2EEPKiPiPS0_ii
    .private_segment_fixed_size: 0
    .sgpr_count:     56
    .sgpr_spill_count: 0
    .symbol:         _Z4k_l2PK15HIP_vector_typeIiLj2EEPKiPiPS0_ii.kd
    .uniform_work_group_size: 1
    .uses_dynamic_stack: false
    .vgpr_count:     96
    .vgpr_spill_count: 0
    .wavefront_size: 64
  - .agpr_count:     0
    .args:
      - .actual_access:  read_only
        .address_space:  global
        .offset:         0
        .size:           8
        .value_kind:     global_buffer
      - .actual_access:  read_only
        .address_space:  global
        .offset:         8
        .size:           8
        .value_kind:     global_buffer
      - .actual_access:  read_only
        .address_space:  global
        .offset:         16
        .size:           8
        .value_kind:     global_buffer
      - .actual_access:  read_only
        .address_space:  global
        .offset:         24
        .size:           8
        .value_kind:     global_buffer
      - .actual_access:  read_only
        .address_space:  global
        .offset:         32
        .size:           8
        .value_kind:     global_buffer
      - .actual_access:  read_only
        .address_space:  global
        .offset:         40
        .size:           8
        .value_kind:     global_buffer
      - .actual_access:  read_only
        .address_space:  global
        .offset:         48
        .size:           8
        .value_kind:     global_buffer
      - .offset:         56
        .size:           4
        .value_kind:     by_value
      - .actual_access:  read_only
        .address_space:  global
        .offset:         64
        .size:           8
        .value_kind:     global_buffer
      - .actual_access:  write_only
        .address_space:  global
        .offset:         72
        .size:           8
        .value_kind:     global_buffer
      - .actual_access:  write_only
        .address_space:  global
        .offset:         80
        .size:           8
        .value_kind:     global_buffer
      - .actual_access:  write_only
        .address_space:  global
        .offset:         88
        .size:           8
        .value_kind:     global_buffer
      - .actual_access:  read_only
        .address_space:  global
        .offset:         96
        .size:           8
        .value_kind:     global_buffer
      - .actual_access:  read_only
        .address_space:  global
        .offset:         104
        .size:           8
        .value_kind:     global_buffer
      - .actual_access:  read_only
        .address_space:  global
        .offset:         112
        .size:           8
        .value_kind:     global_buffer
      - .actual_access:  read_only
        .address_space:  global
        .offset:         120
        .size:           8
        .value_kind:     global_buffer
      - .actual_access:  read_only
        .address_space:  global
        .offset:         128
        .size:           8
        .value_kind:     global_buffer
      - .offset:         136
        .size:           4
        .value_kind:     by_value
      - .offset:         144
        .size:           4
        .value_kind:     hidden_block_count_x
      - .offset:         148
        .size:           4
        .value_kind:     hidden_block_count_y
      - .offset:         152
        .size:           4
        .value_kind:     hidden_block_count_z
      - .offset:         156
        .size:           2
        .value_kind:     hidden_group_size_x
      - .offset:         158
        .size:           2
        .value_kind:     hidden_group_size_y
      - .offset:         160
        .size:           2
        .value_kind:     hidden_group_size_z
      - .offset:         162
        .size:           2
        .value_kind:     hidden_remainder_x
      - .offset:         164
        .size:           2
        .value_kind:     hidden_remainder_y
      - .offset:         166
        .size:           2
        .value_kind:     hidden_remainder_z
      - .offset:         184
        .size:           8
        .value_kind:     hidden_global_offset_x
      - .offset:         192
        .size:           8
        .value_kind:     hidden_global_offset_y
      - .offset:         200
        .size:           8
        .value_kind:     hidden_global_offset_z
      - .offset:         208
        .size:           2
        .value_kind:     hidden_grid_dims
    .group_segment_fixed_size: 20544
    .kernarg_segment_align: 8
    .kernarg_segment_size: 400
    .language:       OpenCL C
    .language_version:
      - 2
      - 0
    .max_flat_workgroup_size: 512
    .name:           _Z6k_spmmILb0ELi0EEvPKiPK15HIP_vector_typeIiLj2EEPKvPKfPKDF16_S9_S9_iPfPDF16_PhSC_PKhS9_SG_S9_S9_i
    .private_segment_fixed_size: 0
    .sgpr_count:     36
    .sgpr_spill_count: 0
    .symbol:         _Z6k_spmmILb0ELi0EEvPKiPK15HIP_vector_typeIiLj2EEPKvPKfPKDF16_S9_S9_iPfPDF16_PhSC_PKhS9_SG_S9_S9_i.kd
    .uniform_work_group_size: 1
    .uses_dynamic_stack: false
    .vgpr_count:     128
    .vgpr_spill_count: 0
    .wavefront_size: 64
  - .agpr_count:     0
    .args:
      - .actual_access:  read_only
        .address_space:  global
        .offset:         0
        .size:           8
        .value_kind:     global_buffer
      - .actual_access:  read_only
        .address_space:  global
        .offset:         8
        .size:           8
        .value_kind:     global_buffer
      - .actual_access:  read_only
        .address_space:  global
        .offset:         16
        .size:           8
        .value_kind:     global_buffer
      - .actual_access:  read_only
        .address_space:  global
        .offset:         24
        .size:           8
        .value_kind:     global_buffer
      - .actual_access:  read_only
        .address_space:  global
        .offset:         32
        .size:           8
        .value_kind:     global_buffer
      - .actual_access:  read_only
        .address_space:  global
        .offset:         40
        .size:           8
        .value_kind:     global_buffer
      - .actual_access:  read_only
        .address_space:  global
        .offset:         48
        .size:           8
        .value_kind:     global_buffer
      - .offset:         56
        .size:           4
        .value_kind:     by_value
      - .actual_access:  read_only
        .address_space:  global
        .offset:         64
        .size:           8
        .value_kind:     global_buffer
      - .actual_access:  read_only
        .address_space:  global
        .offset:         72
        .size:           8
        .value_kind:     global_buffer
      - .actual_access:  write_only
        .address_space:  global
        .offset:         80
        .size:           8
        .value_kind:     global_buffer
      - .actual_access:  write_only
        .address_space:  global
        .offset:         88
        .size:           8
        .value_kind:     global_buffer
      - .actual_access:  read_only
        .address_space:  global
        .offset:         96
        .size:           8
        .value_kind:     global_buffer
      - .actual_access:  read_only
        .address_space:  global
        .offset:         104
        .size:           8
        .value_kind:     global_buffer
      - .actual_access:  read_only
        .address_space:  global
        .offset:         112
        .size:           8
        .value_kind:     global_buffer
      - .actual_access:  read_only
        .address_space:  global
        .offset:         120
        .size:           8
        .value_kind:     global_buffer
      - .actual_access:  read_only
        .address_space:  global
        .offset:         128
        .size:           8
        .value_kind:     global_buffer
      - .offset:         136
        .size:           4
        .value_kind:     by_value
      - .offset:         144
        .size:           4
        .value_kind:     hidden_block_count_x
      - .offset:         148
        .size:           4
        .value_kind:     hidden_block_count_y
      - .offset:         152
        .size:           4
        .value_kind:     hidden_block_count_z
      - .offset:         156
        .size:           2
        .value_kind:     hidden_group_size_x
      - .offset:         158
        .size:           2
        .value_kind:     hidden_group_size_y
      - .offset:         160
        .size:           2
        .value_kind:     hidden_group_size_z
      - .offset:         162
        .size:           2
        .value_kind:     hidden_remainder_x
      - .offset:         164
        .size:           2
        .value_kind:     hidden_remainder_y
      - .offset:         166
        .size:           2
        .value_kind:     hidden_remainder_z
      - .offset:         184
        .size:           8
        .value_kind:     hidden_global_offset_x
      - .offset:         192
        .size:           8
        .value_kind:     hidden_global_offset_y
      - .offset:         200
        .size:           8
        .value_kind:     hidden_global_offset_z
      - .offset:         208
        .size:           2
        .value_kind:     hidden_grid_dims
    .group_segment_fixed_size: 20544
    .kernarg_segment_align: 8
    .kernarg_segment_size: 400
    .language:       OpenCL C
    .language_version:
      - 2
      - 0
    .max_flat_workgroup_size: 512
    .name:           _Z6k_spmmILb1ELi1EEvPKiPK15HIP_vector_typeIiLj2EEPKvPKfPKDF16_S9_S9_iPfPDF16_PhSC_PKhS9_SG_S9_S9_i
    .private_segment_fixed_size: 0
    .sgpr_count:     36
    .sgpr_spill_count: 0
    .symbol:         _Z6k_spmmILb1ELi1EEvPKiPK15HIP_vector_typeIiLj2EEPKvPKfPKDF16_S9_S9_iPfPDF16_PhSC_PKhS9_SG_S9_S9_i.kd
    .uniform_work_group_size: 1
    .uses_dynamic_stack: false
    .vgpr_count:     64
    .vgpr_spill_count: 0
    .wavefront_size: 64
  - .agpr_count:     0
    .args:
      - .actual_access:  read_only
        .address_space:  global
        .offset:         0
        .size:           8
        .value_kind:     global_buffer
      - .actual_access:  read_only
        .address_space:  global
        .offset:         8
        .size:           8
        .value_kind:     global_buffer
      - .actual_access:  read_only
        .address_space:  global
        .offset:         16
        .size:           8
        .value_kind:     global_buffer
      - .actual_access:  read_only
        .address_space:  global
        .offset:         24
        .size:           8
        .value_kind:     global_buffer
      - .actual_access:  read_only
        .address_space:  global
        .offset:         32
        .size:           8
        .value_kind:     global_buffer
      - .actual_access:  read_only
        .address_space:  global
        .offset:         40
        .size:           8
        .value_kind:     global_buffer
      - .actual_access:  read_only
        .address_space:  global
        .offset:         48
        .size:           8
        .value_kind:     global_buffer
      - .offset:         56
        .size:           4
        .value_kind:     by_value
      - .actual_access:  write_only
        .address_space:  global
        .offset:         64
        .size:           8
        .value_kind:     global_buffer
      - .actual_access:  read_only
        .address_space:  global
        .offset:         72
        .size:           8
        .value_kind:     global_buffer
      - .actual_access:  read_only
        .address_space:  global
        .offset:         80
        .size:           8
        .value_kind:     global_buffer
      - .actual_access:  read_only
        .address_space:  global
        .offset:         88
        .size:           8
        .value_kind:     global_buffer
      - .actual_access:  read_only
        .address_space:  global
        .offset:         96
        .size:           8
        .value_kind:     global_buffer
      - .actual_access:  read_only
        .address_space:  global
        .offset:         104
        .size:           8
        .value_kind:     global_buffer
      - .actual_access:  read_only
        .address_space:  global
        .offset:         112
        .size:           8
        .value_kind:     global_buffer
      - .actual_access:  read_only
        .address_space:  global
        .offset:         120
        .size:           8
        .value_kind:     global_buffer
      - .actual_access:  read_only
        .address_space:  global
        .offset:         128
        .size:           8
        .value_kind:     global_buffer
      - .offset:         136
        .size:           4
        .value_kind:     by_value
      - .offset:         144
        .size:           4
        .value_kind:     hidden_block_count_x
      - .offset:         148
        .size:           4
        .value_kind:     hidden_block_count_y
      - .offset:         152
        .size:           4
        .value_kind:     hidden_block_count_z
      - .offset:         156
        .size:           2
        .value_kind:     hidden_group_size_x
      - .offset:         158
        .size:           2
        .value_kind:     hidden_group_size_y
      - .offset:         160
        .size:           2
        .value_kind:     hidden_group_size_z
      - .offset:         162
        .size:           2
        .value_kind:     hidden_remainder_x
      - .offset:         164
        .size:           2
        .value_kind:     hidden_remainder_y
      - .offset:         166
        .size:           2
        .value_kind:     hidden_remainder_z
      - .offset:         184
        .size:           8
        .value_kind:     hidden_global_offset_x
      - .offset:         192
        .size:           8
        .value_kind:     hidden_global_offset_y
      - .offset:         200
        .size:           8
        .value_kind:     hidden_global_offset_z
      - .offset:         208
        .size:           2
        .value_kind:     hidden_grid_dims
    .group_segment_fixed_size: 20480
    .kernarg_segment_align: 8
    .kernarg_segment_size: 400
    .language:       OpenCL C
    .language_version:
      - 2
      - 0
    .max_flat_workgroup_size: 512
    .name:           _Z6k_spmmILb1ELi2EEvPKiPK15HIP_vector_typeIiLj2EEPKvPKfPKDF16_S9_S9_iPfPDF16_PhSC_PKhS9_SG_S9_S9_i
    .private_segment_fixed_size: 0
    .sgpr_count:     42
    .sgpr_spill_count: 0
    .symbol:         _Z6k_spmmILb1ELi2EEvPKiPK15HIP_vector_typeIiLj2EEPKvPKfPKDF16_S9_S9_iPfPDF16_PhSC_PKhS9_SG_S9_S9_i.kd
    .uniform_work_group_size: 1
    .uses_dynamic_stack: false
    .vgpr_count:     64
    .vgpr_spill_count: 0
    .wavefront_size: 64
